# mask hand-off: remaining plain mask stores write-through, publisher's L2 write-back removed
# speedup vs baseline: 1.0057x; 1.0057x over previous
; __device__ __forceinline__ unsigned swap_or(unsigned v) { auto rr = __builtin_amdgcn_permlane32_swap(v, v, false, false); return rr[0] | rr[1]; }
; __device__ __forceinline__ void idx_unit(int b, int qb, const bf16_t* QI, const bf16_t* KI, const float* WI, unsigned long long* mask, LAS unsigned* hist, int tid) {
;     ...
;         }
;         lo = swap_or(lo); hw = swap_or(hw);
;         if (hi == 0) mask[row * 64 + j] = (unsigned long long)lo | ((unsigned long long)hw << 32);
.LBB0_1031:
	v_mov_b32_e32 v3, v236
	v_mov_b32_e32 v4, v2
	s_nop 0
	v_permlane32_swap_b32_e32 v236, v3
	v_permlane32_swap_b32_e32 v2, v4
	s_and_saveexec_b64 s[14:15], s[8:9]
	s_cbranch_execz .LBB0_930
	s_ashr_i32 s43, s42, 31
	v_or_b32_e32 v5, v2, v4
	v_or_b32_e32 v4, v236, v3
	v_lshl_add_u64 v[2:3], s[42:43], 3, v[210:211]
	global_store_dwordx2 v[2:3], v[4:5], off sc1
	s_branch .LBB0_930

; __device__ __forceinline__ bool idx_unit_fast(int b, int qb, const bf16_t* QI, const bf16_t* KI, const float* WI, unsigned long long* mask, LAS unsigned char* L, int tid) {
;     ...
;     if (t0 < 256) {
;         const int r = tid >> 4, j = tid & 15, t = t0 + r;
;         if (j <= jtop) { const int n = t - 64 * j + 1; const unsigned long long m = n >= 64 ? ~0ull : (n <= 0 ? 0ull : ((1ull << n) - 1ull)); mask[(rowbase + t) * 64 + j] = m; }
;         return false;
.LBB0_1641:
	s_and_b64 vcc, exec, s[10:11]
	s_cbranch_vccz .LBB0_1645
	v_and_b32_e32 v0, 15, v220
	v_cmp_ge_u32_e32 vcc, s63, v0
	s_and_saveexec_b64 s[10:11], vcc
	s_cbranch_execz .LBB0_1644
	v_ashrrev_i32_e32 v2, 4, v220
	v_add_u32_e32 v2, s62, v2
	v_lshlrev_b32_e32 v3, 6, v0
	v_sub_u32_e32 v3, v2, v3
	v_add_u32_e32 v4, 1, v3
	v_lshlrev_b64 v[4:5], v4, -1
	v_not_b32_e32 v5, v5
	v_not_b32_e32 v4, v4
	v_cmp_lt_i32_e32 vcc, -1, v3
	v_lshlrev_b32_e32 v0, 3, v0
	s_nop 0
	v_cndmask_b32_e32 v4, 0, v4, vcc
	v_cndmask_b32_e32 v5, 0, v5, vcc
	v_cmp_gt_i32_e32 vcc, 63, v3
	v_ashrrev_i32_e32 v3, 31, v2
	v_lshl_add_u64 v[2:3], s[36:37], 0, v[2:3]
	v_lshlrev_b64 v[2:3], 9, v[2:3]
	v_lshl_add_u64 v[2:3], s[34:35], 0, v[2:3]
	v_cndmask_b32_e32 v5, -1, v5, vcc
	v_cndmask_b32_e32 v4, -1, v4, vcc
	v_lshl_add_u64 v[2:3], v[2:3], 0, v[0:1]
	global_store_dwordx2 v[2:3], v[4:5], off sc1

; __device__ __forceinline__ int lane_id() { int l; asm volatile("v_mbcnt_lo_u32_b32 %0, -1, 0\n\tv_mbcnt_hi_u32_b32 %0, -1, %0" : "=v"(l)); return l; }
; __device__ __forceinline__ unsigned char* karg_ws() { return (unsigned char*)(GAS unsigned char*)karg_u64<15>(); }
; __device__ __forceinline__ void mflag_publish(int b, int qb, unsigned tag, int wave_s) {
;     asm volatile("s_waitcnt vmcnt(0)" ::: "memory");
;     __syncthreads();
;     if (wave_s == 0 && lane_id() == 0) {
;         __builtin_amdgcn_fence(__ATOMIC_RELEASE, "agent");
;         asm volatile("s_waitcnt vmcnt(0)" ::: "memory");
;         __hip_atomic_store((unsigned*)(karg_ws() + WS_CTL) + CTL_MFLAG + 16 * (128 * b + qb), tag, __ATOMIC_RELAXED, __HIP_MEMORY_SCOPE_AGENT);
;     }
; }
.LBB0_1645:
	s_waitcnt vmcnt(0)
	s_andn2_b64 vcc, exec, s[80:81]
	s_barrier
	s_cbranch_vccnz .LBB0_697
	v_mbcnt_lo_u32_b32 v0, -1, 0
	v_mbcnt_hi_u32_b32 v0, -1, v0
	s_nop 0
	v_cmp_eq_u32_e32 vcc, 0, v0
	s_and_saveexec_b64 s[10:11], vcc
	s_cbranch_execz .LBB0_696
	s_lshl_b32 s2, s61, 4
	s_or_b32 s2, s2, s60
	s_waitcnt vmcnt(0)
	s_waitcnt vmcnt(0)
	s_ashr_i32 s3, s2, 31
	s_load_dwordx2 s[0:1], s[76:77], 0x78
	s_waitcnt lgkmcnt(0)
	s_lshl_b64 s[2:3], s[2:3], 2
	s_add_u32 s0, s0, s2
	s_addc_u32 s1, s1, s3
	v_mov_b32_e32 v0, 0x8000
	global_store_dword v0, v239, s[0:1] sc1
	s_branch .LBB0_696
